# P7 residual epilogue: all 16 base-tile loads batched up front into dead fragment registers with counted vmcnt (was 16 serialized load-wait-store round trips)
# baseline (speedup 1.0000x reference)
.LBB0_727:
	v_lshl_add_u32 v148, s28, 8, v150
	v_lshl_or_b32 v146, s55, 8, v152
	v_ashrrev_i32_e32 v149, 31, v148
	v_ashrrev_i32_e32 v147, 31, v146
	v_lshlrev_b64 v[144:145], 12, v[148:149]
	v_lshl_add_u64 v[144:145], v[144:145], 0, v[146:147]
	v_lshlrev_b64 v[144:145], 1, v[144:145]
	v_lshl_add_u64 v[160:161], s[2:3], 0, v[144:145]
	s_mov_b32 s98, 0x20000
	s_mov_b32 s99, 0
	s_mov_b32 s100, 0xa0000
	s_mov_b32 s101, 0
	v_mov_b64_e32 v[252:253], v[160:161]
	global_load_dwordx4 v[168:171], v[252:253], off
	global_load_dwordx4 v[172:175], v[252:253], off offset:256
	v_lshl_add_u64 v[252:253], v[252:253], 0, s[98:99]
	global_load_dwordx4 v[176:179], v[252:253], off
	global_load_dwordx4 v[180:183], v[252:253], off offset:256
	v_lshl_add_u64 v[252:253], v[252:253], 0, s[98:99]
	global_load_dwordx4 v[184:187], v[252:253], off
	global_load_dwordx4 v[188:191], v[252:253], off offset:256
	v_lshl_add_u64 v[252:253], v[252:253], 0, s[98:99]
	global_load_dwordx4 v[192:195], v[252:253], off
	global_load_dwordx4 v[196:199], v[252:253], off offset:256
	v_lshl_add_u64 v[252:253], v[252:253], 0, s[100:101]
	global_load_dwordx4 v[200:203], v[252:253], off
	global_load_dwordx4 v[204:207], v[252:253], off offset:256
	v_lshl_add_u64 v[252:253], v[252:253], 0, s[98:99]
	global_load_dwordx4 v[208:211], v[252:253], off
	global_load_dwordx4 v[212:215], v[252:253], off offset:256
	v_lshl_add_u64 v[252:253], v[252:253], 0, s[98:99]
	global_load_dwordx4 v[216:219], v[252:253], off
	global_load_dwordx4 v[232:235], v[252:253], off offset:256
	v_lshl_add_u64 v[252:253], v[252:253], 0, s[98:99]
	global_load_dwordx4 v[236:239], v[252:253], off
	global_load_dwordx4 v[240:243], v[252:253], off offset:256
	s_andn2_b64 vcc, exec, s[4:5]
	s_mov_b64 s[4:5], -1
	s_nop 0
	s_waitcnt vmcnt(15)
	v_lshlrev_b32_e32 v149, 16, v168
	v_and_b32_e32 v156, 0xffff0000, v168
	v_lshlrev_b32_e32 v162, 16, v169
	v_and_b32_e32 v157, 0xffff0000, v169
	v_lshlrev_b32_e32 v164, 16, v171
	v_and_b32_e32 v159, 0xffff0000, v171
	v_lshlrev_b32_e32 v163, 16, v170
	v_and_b32_e32 v158, 0xffff0000, v170
	v_add_f32_e32 v124, v124, v149
	v_add_f32_e32 v125, v125, v156
	v_add_f32_e32 v126, v126, v162
	v_add_f32_e32 v127, v127, v157
	v_add_f32_e32 v123, v123, v159
	v_add_f32_e32 v149, v120, v163
	v_add_f32_e32 v156, v121, v158
	v_add_f32_e32 v157, v122, v164
	v_cvt_pk_bf16_f32 v120, v124, v125
	v_cvt_pk_bf16_f32 v121, v126, v127
	v_cvt_pk_bf16_f32 v122, v149, v156
	v_cvt_pk_bf16_f32 v123, v157, v123
	v_or_b32_e32 v156, 16, v148
	v_ashrrev_i32_e32 v157, 31, v156
	v_lshlrev_b64 v[156:157], 12, v[156:157]
	v_lshl_add_u64 v[158:159], s[6:7], 0, v[144:145]
	v_lshl_add_u64 v[156:157], v[156:157], 0, v[146:147]
	global_store_dwordx4 v[158:159], v[120:123], off
	v_lshlrev_b64 v[156:157], 1, v[156:157]
	v_lshl_add_u64 v[160:161], s[2:3], 0, v[156:157]
	s_nop 0
	s_waitcnt vmcnt(15)
	v_lshlrev_b32_e32 v120, 16, v172
	v_and_b32_e32 v121, 0xffff0000, v172
	v_lshlrev_b32_e32 v122, 16, v173
	v_and_b32_e32 v123, 0xffff0000, v173
	v_lshlrev_b32_e32 v124, 16, v174
	v_and_b32_e32 v125, 0xffff0000, v174
	v_lshlrev_b32_e32 v126, 16, v175
	v_and_b32_e32 v127, 0xffff0000, v175
	v_add_f32_e32 v111, v111, v127
	v_add_f32_e32 v116, v116, v120
	v_add_f32_e32 v117, v117, v121
	v_add_f32_e32 v118, v118, v122
	v_add_f32_e32 v119, v119, v123
	v_add_f32_e32 v120, v108, v124
	v_add_f32_e32 v121, v109, v125
	v_add_f32_e32 v122, v110, v126
	v_cvt_pk_bf16_f32 v108, v116, v117
	v_cvt_pk_bf16_f32 v109, v118, v119
	v_cvt_pk_bf16_f32 v110, v120, v121
	v_cvt_pk_bf16_f32 v111, v122, v111
	global_store_dwordx4 v[158:159], v[108:111], off offset:256
	s_nop 0
	s_waitcnt vmcnt(15)
	v_lshlrev_b32_e32 v116, 16, v176
	v_and_b32_e32 v108, 0xffff0000, v176
	v_lshlrev_b32_e32 v117, 16, v177
	v_and_b32_e32 v109, 0xffff0000, v177
	v_lshlrev_b32_e32 v118, 16, v178
	v_and_b32_e32 v110, 0xffff0000, v178
	v_lshlrev_b32_e32 v119, 16, v179
	v_and_b32_e32 v111, 0xffff0000, v179
	v_add_f32_e32 v108, v113, v108
	v_add_f32_e32 v109, v115, v109
	v_add_f32_e32 v110, v105, v110
	v_add_f32_e32 v107, v107, v111
	v_add_f32_e32 v112, v112, v116
	v_add_f32_e32 v113, v114, v117
	v_add_f32_e32 v114, v104, v118
	v_add_f32_e32 v115, v106, v119
	v_cvt_pk_bf16_f32 v104, v112, v108
	v_cvt_pk_bf16_f32 v105, v113, v109
	v_cvt_pk_bf16_f32 v106, v114, v110
	v_cvt_pk_bf16_f32 v107, v115, v107
	v_or_b32_e32 v112, 32, v148
	v_ashrrev_i32_e32 v113, 31, v112
	v_lshlrev_b64 v[112:113], 12, v[112:113]
	v_lshl_add_u64 v[114:115], s[6:7], 0, v[156:157]
	v_lshl_add_u64 v[112:113], v[112:113], 0, v[146:147]
	global_store_dwordx4 v[114:115], v[104:107], off
	v_lshlrev_b64 v[112:113], 1, v[112:113]
	v_lshl_add_u64 v[116:117], s[2:3], 0, v[112:113]
	s_nop 0
	s_waitcnt vmcnt(15)
	v_lshlrev_b32_e32 v104, 16, v180
	v_and_b32_e32 v105, 0xffff0000, v180
	v_lshlrev_b32_e32 v106, 16, v181
	v_and_b32_e32 v107, 0xffff0000, v181
	v_lshlrev_b32_e32 v108, 16, v182
	v_and_b32_e32 v109, 0xffff0000, v182
	v_lshlrev_b32_e32 v110, 16, v183
	v_and_b32_e32 v111, 0xffff0000, v183
	v_add_f32_e32 v95, v95, v111
	v_add_f32_e32 v100, v100, v104
	v_add_f32_e32 v101, v101, v105
	v_add_f32_e32 v102, v102, v106
	v_add_f32_e32 v103, v103, v107
	v_add_f32_e32 v104, v92, v108
	v_add_f32_e32 v105, v93, v109
	v_add_f32_e32 v106, v94, v110
	v_cvt_pk_bf16_f32 v92, v100, v101
	v_cvt_pk_bf16_f32 v93, v102, v103
	v_cvt_pk_bf16_f32 v94, v104, v105
	v_cvt_pk_bf16_f32 v95, v106, v95
	global_store_dwordx4 v[114:115], v[92:95], off offset:256
	s_nop 0
	s_waitcnt vmcnt(15)
	v_lshlrev_b32_e32 v100, 16, v184
	v_and_b32_e32 v92, 0xffff0000, v184
	v_lshlrev_b32_e32 v101, 16, v185
	v_and_b32_e32 v93, 0xffff0000, v185
	v_lshlrev_b32_e32 v102, 16, v186
	v_and_b32_e32 v94, 0xffff0000, v186
	v_lshlrev_b32_e32 v103, 16, v187
	v_and_b32_e32 v95, 0xffff0000, v187
	v_add_f32_e32 v92, v97, v92
	v_add_f32_e32 v93, v99, v93
	v_add_f32_e32 v94, v89, v94
	v_add_f32_e32 v91, v91, v95
	v_add_f32_e32 v96, v96, v100
	v_add_f32_e32 v97, v98, v101
	v_add_f32_e32 v98, v88, v102
	v_add_f32_e32 v99, v90, v103
	v_cvt_pk_bf16_f32 v88, v96, v92
	v_cvt_pk_bf16_f32 v89, v97, v93
	v_cvt_pk_bf16_f32 v90, v98, v94
	v_cvt_pk_bf16_f32 v91, v99, v91
	v_or_b32_e32 v96, 48, v148
	v_ashrrev_i32_e32 v97, 31, v96
	v_lshlrev_b64 v[96:97], 12, v[96:97]
	v_lshl_add_u64 v[98:99], s[6:7], 0, v[112:113]
	v_lshl_add_u64 v[96:97], v[96:97], 0, v[146:147]
	global_store_dwordx4 v[98:99], v[88:91], off
	v_lshlrev_b64 v[96:97], 1, v[96:97]
	v_lshl_add_u64 v[100:101], s[2:3], 0, v[96:97]
	s_nop 0
	s_waitcnt vmcnt(15)
	v_lshlrev_b32_e32 v88, 16, v188
	v_and_b32_e32 v89, 0xffff0000, v188
	v_lshlrev_b32_e32 v90, 16, v189
	v_and_b32_e32 v91, 0xffff0000, v189
	v_lshlrev_b32_e32 v92, 16, v190
	v_and_b32_e32 v93, 0xffff0000, v190
	v_lshlrev_b32_e32 v94, 16, v191
	v_and_b32_e32 v95, 0xffff0000, v191
	v_add_f32_e32 v79, v79, v95
	v_add_f32_e32 v84, v84, v88
	v_add_f32_e32 v85, v85, v89
	v_add_f32_e32 v86, v86, v90
	v_add_f32_e32 v87, v87, v91
	v_add_f32_e32 v88, v76, v92
	v_add_f32_e32 v89, v77, v93
	v_add_f32_e32 v90, v78, v94
	v_cvt_pk_bf16_f32 v76, v84, v85
	v_cvt_pk_bf16_f32 v77, v86, v87
	v_cvt_pk_bf16_f32 v78, v88, v89
	v_cvt_pk_bf16_f32 v79, v90, v79
	global_store_dwordx4 v[98:99], v[76:79], off offset:256
	s_nop 0
	s_waitcnt vmcnt(15)
	v_lshlrev_b32_e32 v84, 16, v192
	v_and_b32_e32 v76, 0xffff0000, v192
	v_lshlrev_b32_e32 v85, 16, v193
	v_and_b32_e32 v77, 0xffff0000, v193
	v_lshlrev_b32_e32 v86, 16, v194
	v_and_b32_e32 v78, 0xffff0000, v194
	v_lshlrev_b32_e32 v87, 16, v195
	v_and_b32_e32 v79, 0xffff0000, v195
	v_add_f32_e32 v76, v81, v76
	v_add_f32_e32 v77, v83, v77
	v_add_f32_e32 v78, v73, v78
	v_add_f32_e32 v75, v75, v79
	v_add_f32_e32 v80, v80, v84
	v_add_f32_e32 v81, v82, v85
	v_add_f32_e32 v82, v72, v86
	v_add_f32_e32 v83, v74, v87
	v_cvt_pk_bf16_f32 v72, v80, v76
	v_cvt_pk_bf16_f32 v73, v81, v77
	v_cvt_pk_bf16_f32 v74, v82, v78
	v_cvt_pk_bf16_f32 v75, v83, v75
	v_lshl_add_u64 v[82:83], s[6:7], 0, v[96:97]
	global_store_dwordx4 v[82:83], v[72:75], off
	v_lshl_add_u64 v[80:81], v[144:145], 0, s[12:13]
	v_lshl_add_u64 v[84:85], s[2:3], 0, v[80:81]
	s_nop 0
	s_waitcnt vmcnt(15)
	v_lshlrev_b32_e32 v72, 16, v196
	v_and_b32_e32 v73, 0xffff0000, v196
	v_lshlrev_b32_e32 v74, 16, v197
	v_and_b32_e32 v75, 0xffff0000, v197
	v_lshlrev_b32_e32 v76, 16, v198
	v_and_b32_e32 v77, 0xffff0000, v198
	v_lshlrev_b32_e32 v78, 16, v199
	v_and_b32_e32 v79, 0xffff0000, v199
	v_add_f32_e32 v67, v67, v79
	v_add_f32_e32 v68, v68, v72
	v_add_f32_e32 v69, v69, v73
	v_add_f32_e32 v70, v70, v74
	v_add_f32_e32 v71, v71, v75
	v_add_f32_e32 v72, v64, v76
	v_add_f32_e32 v73, v65, v77
	v_add_f32_e32 v74, v66, v78
	v_cvt_pk_bf16_f32 v64, v68, v69
	v_cvt_pk_bf16_f32 v65, v70, v71
	v_cvt_pk_bf16_f32 v66, v72, v73
	v_cvt_pk_bf16_f32 v67, v74, v67
	global_store_dwordx4 v[82:83], v[64:67], off offset:256
	s_nop 0
	s_waitcnt vmcnt(15)
	v_lshlrev_b32_e32 v68, 16, v200
	v_and_b32_e32 v64, 0xffff0000, v200
	v_lshlrev_b32_e32 v69, 16, v201
	v_and_b32_e32 v65, 0xffff0000, v201
	v_lshlrev_b32_e32 v71, 16, v203
	v_and_b32_e32 v67, 0xffff0000, v203
	v_lshlrev_b32_e32 v70, 16, v202
	v_and_b32_e32 v66, 0xffff0000, v202
	v_add_f32_e32 v60, v60, v68
	v_add_f32_e32 v61, v61, v64
	v_add_f32_e32 v62, v62, v69
	v_add_f32_e32 v63, v63, v65
	v_add_f32_e32 v59, v59, v67
	v_add_f32_e32 v64, v56, v70
	v_add_f32_e32 v65, v57, v66
	v_add_f32_e32 v66, v58, v71
	v_cvt_pk_bf16_f32 v56, v60, v61
	v_cvt_pk_bf16_f32 v57, v62, v63
	v_cvt_pk_bf16_f32 v58, v64, v65
	v_cvt_pk_bf16_f32 v59, v66, v59
	v_lshl_add_u64 v[66:67], s[6:7], 0, v[80:81]
	global_store_dwordx4 v[66:67], v[56:59], off
	v_lshl_add_u64 v[64:65], v[144:145], 0, s[14:15]
	v_lshl_add_u64 v[68:69], s[2:3], 0, v[64:65]
	s_nop 0
	s_waitcnt vmcnt(15)
	v_lshlrev_b32_e32 v56, 16, v204
	v_and_b32_e32 v57, 0xffff0000, v204
	v_lshlrev_b32_e32 v58, 16, v205
	v_and_b32_e32 v59, 0xffff0000, v205
	v_lshlrev_b32_e32 v60, 16, v206
	v_and_b32_e32 v61, 0xffff0000, v206
	v_lshlrev_b32_e32 v62, 16, v207
	v_and_b32_e32 v63, 0xffff0000, v207
	v_add_f32_e32 v47, v47, v63
	v_add_f32_e32 v52, v52, v56
	v_add_f32_e32 v53, v53, v57
	v_add_f32_e32 v54, v54, v58
	v_add_f32_e32 v55, v55, v59
	v_add_f32_e32 v56, v44, v60
	v_add_f32_e32 v57, v45, v61
	v_add_f32_e32 v58, v46, v62
	v_cvt_pk_bf16_f32 v44, v52, v53
	v_cvt_pk_bf16_f32 v45, v54, v55
	v_cvt_pk_bf16_f32 v46, v56, v57
	v_cvt_pk_bf16_f32 v47, v58, v47
	global_store_dwordx4 v[66:67], v[44:47], off offset:256
	s_nop 0
	s_waitcnt vmcnt(15)
	v_lshlrev_b32_e32 v52, 16, v208
	v_and_b32_e32 v44, 0xffff0000, v208
	v_lshlrev_b32_e32 v53, 16, v209
	v_and_b32_e32 v45, 0xffff0000, v209
	v_lshlrev_b32_e32 v54, 16, v210
	v_and_b32_e32 v46, 0xffff0000, v210
	v_lshlrev_b32_e32 v55, 16, v211
	v_and_b32_e32 v47, 0xffff0000, v211
	v_add_f32_e32 v44, v49, v44
	v_add_f32_e32 v45, v51, v45
	v_add_f32_e32 v46, v41, v46
	v_add_f32_e32 v43, v43, v47
	v_add_f32_e32 v48, v48, v52
	v_add_f32_e32 v49, v50, v53
	v_add_f32_e32 v50, v40, v54
	v_add_f32_e32 v51, v42, v55
	v_cvt_pk_bf16_f32 v40, v48, v44
	v_cvt_pk_bf16_f32 v41, v49, v45
	v_cvt_pk_bf16_f32 v42, v50, v46
	v_cvt_pk_bf16_f32 v43, v51, v43
	v_lshl_add_u64 v[50:51], s[6:7], 0, v[64:65]
	global_store_dwordx4 v[50:51], v[40:43], off
	v_lshl_add_u64 v[48:49], v[144:145], 0, s[16:17]
	v_lshl_add_u64 v[52:53], s[2:3], 0, v[48:49]
	s_nop 0
	s_waitcnt vmcnt(15)
	v_lshlrev_b32_e32 v40, 16, v212
	v_and_b32_e32 v41, 0xffff0000, v212
	v_lshlrev_b32_e32 v42, 16, v213
	v_and_b32_e32 v43, 0xffff0000, v213
	v_lshlrev_b32_e32 v44, 16, v214
	v_and_b32_e32 v45, 0xffff0000, v214
	v_lshlrev_b32_e32 v46, 16, v215
	v_and_b32_e32 v47, 0xffff0000, v215
	v_add_f32_e32 v31, v31, v47
	v_add_f32_e32 v36, v36, v40
	v_add_f32_e32 v37, v37, v41
	v_add_f32_e32 v38, v38, v42
	v_add_f32_e32 v39, v39, v43
	v_add_f32_e32 v40, v28, v44
	v_add_f32_e32 v41, v29, v45
	v_add_f32_e32 v42, v30, v46
	v_cvt_pk_bf16_f32 v28, v36, v37
	v_cvt_pk_bf16_f32 v29, v38, v39
	v_cvt_pk_bf16_f32 v30, v40, v41
	v_cvt_pk_bf16_f32 v31, v42, v31
	global_store_dwordx4 v[50:51], v[28:31], off offset:256
	s_nop 0
	s_waitcnt vmcnt(15)
	v_lshlrev_b32_e32 v36, 16, v216
	v_and_b32_e32 v28, 0xffff0000, v216
	v_lshlrev_b32_e32 v37, 16, v217
	v_and_b32_e32 v29, 0xffff0000, v217
	v_lshlrev_b32_e32 v38, 16, v218
	v_and_b32_e32 v30, 0xffff0000, v218
	v_lshlrev_b32_e32 v39, 16, v219
	v_and_b32_e32 v31, 0xffff0000, v219
	v_add_f32_e32 v28, v33, v28
	v_add_f32_e32 v29, v35, v29
	v_add_f32_e32 v30, v25, v30
	v_add_f32_e32 v27, v27, v31
	v_add_f32_e32 v32, v32, v36
	v_add_f32_e32 v33, v34, v37
	v_add_f32_e32 v34, v24, v38
	v_add_f32_e32 v35, v26, v39
	v_cvt_pk_bf16_f32 v24, v32, v28
	v_cvt_pk_bf16_f32 v25, v33, v29
	v_cvt_pk_bf16_f32 v26, v34, v30
	v_cvt_pk_bf16_f32 v27, v35, v27
	v_lshl_add_u64 v[34:35], s[6:7], 0, v[48:49]
	global_store_dwordx4 v[34:35], v[24:27], off
	v_lshl_add_u64 v[32:33], v[144:145], 0, s[18:19]
	v_lshl_add_u64 v[36:37], s[2:3], 0, v[32:33]
	s_nop 0
	s_waitcnt vmcnt(15)
	v_lshlrev_b32_e32 v24, 16, v232
	v_and_b32_e32 v25, 0xffff0000, v232
	v_lshlrev_b32_e32 v26, 16, v233
	v_and_b32_e32 v27, 0xffff0000, v233
	v_lshlrev_b32_e32 v28, 16, v234
	v_and_b32_e32 v29, 0xffff0000, v234
	v_lshlrev_b32_e32 v30, 16, v235
	v_and_b32_e32 v31, 0xffff0000, v235
	v_add_f32_e32 v15, v15, v31
	v_add_f32_e32 v20, v20, v24
	v_add_f32_e32 v21, v21, v25
	v_add_f32_e32 v22, v22, v26
	v_add_f32_e32 v23, v23, v27
	v_add_f32_e32 v24, v12, v28
	v_add_f32_e32 v25, v13, v29
	v_add_f32_e32 v26, v14, v30
	v_cvt_pk_bf16_f32 v12, v20, v21
	v_cvt_pk_bf16_f32 v13, v22, v23
	v_cvt_pk_bf16_f32 v14, v24, v25
	v_cvt_pk_bf16_f32 v15, v26, v15
	global_store_dwordx4 v[34:35], v[12:15], off offset:256
	s_nop 0
	s_waitcnt vmcnt(15)
	v_lshlrev_b32_e32 v20, 16, v236
	v_and_b32_e32 v12, 0xffff0000, v236
	v_lshlrev_b32_e32 v21, 16, v237
	v_and_b32_e32 v13, 0xffff0000, v237
	v_lshlrev_b32_e32 v22, 16, v238
	v_and_b32_e32 v14, 0xffff0000, v238
	v_lshlrev_b32_e32 v23, 16, v239
	v_and_b32_e32 v15, 0xffff0000, v239
	v_add_f32_e32 v12, v17, v12
	v_add_f32_e32 v13, v19, v13
	v_add_f32_e32 v14, v9, v14
	v_add_f32_e32 v11, v11, v15
	v_add_f32_e32 v16, v16, v20
	v_add_f32_e32 v17, v18, v21
	v_add_f32_e32 v18, v8, v22
	v_add_f32_e32 v19, v10, v23
	v_cvt_pk_bf16_f32 v8, v16, v12
	v_cvt_pk_bf16_f32 v9, v17, v13
	v_cvt_pk_bf16_f32 v10, v18, v14
	v_cvt_pk_bf16_f32 v11, v19, v11
	v_lshl_add_u64 v[16:17], s[6:7], 0, v[32:33]
	global_store_dwordx4 v[16:17], v[8:11], off
	s_nop 0
	s_nop 0
	s_waitcnt vmcnt(15)
	v_lshlrev_b32_e32 v8, 16, v240
	v_and_b32_e32 v9, 0xffff0000, v240
	v_lshlrev_b32_e32 v10, 16, v241
	v_and_b32_e32 v11, 0xffff0000, v241
	v_lshlrev_b32_e32 v12, 16, v242
	v_and_b32_e32 v13, 0xffff0000, v242
	v_lshlrev_b32_e32 v14, 16, v243
	v_and_b32_e32 v15, 0xffff0000, v243
	v_add_f32_e32 v3, v3, v15
	v_add_f32_e32 v4, v4, v8
	v_add_f32_e32 v5, v5, v9
	v_add_f32_e32 v6, v6, v10
	v_add_f32_e32 v7, v7, v11
	v_add_f32_e32 v8, v0, v12
	v_add_f32_e32 v9, v1, v13
	v_add_f32_e32 v10, v2, v14
	v_cvt_pk_bf16_f32 v0, v4, v5
	v_cvt_pk_bf16_f32 v1, v6, v7
	v_cvt_pk_bf16_f32 v2, v8, v9
	v_cvt_pk_bf16_f32 v3, v10, v3
	global_store_dwordx4 v[16:17], v[0:3], off offset:256
	s_cbranch_vccnz .LBB0_716
	s_andn2_b64 vcc, exec, s[0:1]
	s_cbranch_vccnz .LBB0_715
	s_barrier
	s_branch .LBB0_715
